# top-k problems re-assigned so each (expert,batch) list is produced on the XCD whose FFN-up units consume it; layer 0's top-k -> FFN-up barrier takes the XCD-local path (layer 1's stays full because th
# speedup vs baseline: 1.0038x; 1.0002x over previous
.LBB0_787:
	s_or_b64 exec, exec, s[30:31]
	v_readlane_b32 s4, v253, 40
	v_mov_b32_e32 v135, v0
	s_mov_b64 s[0:1], 0
	s_mov_b32 s24, s37
	v_readlane_b32 s27, v253, 8
	v_readlane_b32 s18, v253, 54
	s_waitcnt lgkmcnt(0)
	s_barrier
	v_readlane_b32 s19, v253, 55
	s_add_u32 s62, s18, s0
	s_addc_u32 s26, s19, s1
	v_and_b32_e32 v132, 63, v135
	s_cmp_lt_i32 s27, 32
	s_mov_b64 s[0:1], -1
	v_readlane_b32 s5, v253, 41
	v_readlane_b32 s6, v253, 42
	v_readlane_b32 s7, v253, 43
	v_readlane_b32 s8, v253, 44
	v_readlane_b32 s9, v253, 45
	v_readlane_b32 s10, v253, 46
	v_readlane_b32 s11, v253, 47
	v_readlane_b32 s12, v253, 48
	v_readlane_b32 s13, v253, 49
	v_readlane_b32 s14, v253, 50
	v_readlane_b32 s15, v253, 51
	v_readlane_b32 s16, v253, 52
	v_readlane_b32 s17, v253, 53
	s_cbranch_scc0 .LBB0_876
	s_and_b32 s0, s27, 7
	s_lshr_b32 s1, s27, 3
	s_lshl_b32 s0, s0, 2
	s_or_b32 s27, s0, s1
	s_and_b32 s37, s27, 1
	s_ashr_i32 s25, s27, 1
	s_lshl_b32 s0, s37, 4
	s_add_i32 s0, s0, s25
	s_ashr_i32 s1, s0, 31
	s_lshl_b64 s[0:1], s[0:1], 16
	s_add_u32 s0, s62, s0
	v_lshlrev_b32_e32 v34, 5, v135
	s_addc_u32 s1, s26, s1
	v_ashrrev_i32_e32 v35, 31, v34
	v_lshl_add_u64 v[2:3], v[34:35], 2, s[0:1]
	s_mov_b64 s[0:1], 0x200000
	v_lshl_add_u64 v[4:5], v[2:3], 0, s[0:1]
	s_mov_b32 s0, 0x200000
	v_add_co_u32_e32 v2, vcc, s0, v2
	s_mov_b32 s2, 0
	s_nop 0
	v_addc_co_u32_e32 v3, vcc, 0, v3, vcc
	global_load_dwordx4 v[26:29], v[4:5], off offset:16
	global_load_dwordx4 v[22:25], v[4:5], off offset:32
	global_load_dwordx4 v[18:21], v[4:5], off offset:48
	global_load_dwordx4 v[14:17], v[4:5], off offset:64
	global_load_dwordx4 v[10:13], v[4:5], off offset:80
	global_load_dwordx4 v[6:9], v[4:5], off offset:96
	global_load_dwordx4 v[30:33], v[2:3], off
	s_nop 0
	global_load_dwordx4 v[2:5], v[4:5], off offset:112
	v_cmp_eq_u32_e32 vcc, 0, v132
	s_mov_b32 s3, 29
	v_mov_b32_e32 v45, 0
	s_branch .LBB0_790

.LBB0_910:
	s_mov_b64 s[2:3], exec
	s_lshl_b32 s0, s36, 8
	v_readlane_b32 s4, v253, 2
	v_mbcnt_lo_u32_b32 v3, s2, 0
	v_readlane_b32 s5, v253, 3
	s_add_u32 s0, s4, s0
	v_mbcnt_hi_u32_b32 v3, s3, v3
	s_addc_u32 s1, s5, 0
	v_mov_b32_e32 v21, 0x300
	s_nop 4
	global_load_dword v20, v21, s[4:5] sc1
	v_cmp_eq_u32_e32 vcc, 0, v3
	s_and_saveexec_b64 s[4:5], vcc
	s_cbranch_execz .LBB0_912
	s_bcnt1_i32_b64 s2, s[2:3]
	v_mov_b32_e32 v5, s2
	v_mov_b32_e32 v6, 0x1000
	global_atomic_add v5, v6, v5, s[0:1] offset:1024 sc0
.LBB0_912:
	s_or_b64 exec, exec, s[4:5]
	s_waitcnt vmcnt(0)
	v_readfirstlane_b32 s2, v5
	v_sub_u32_e32 v6, 0, v4
	s_nop 0
	v_add_u32_e32 v5, s2, v3
	v_cvt_f32_u32_e32 v3, v4
	v_rcp_iflag_f32_e32 v3, v3
	s_nop 0
	v_mul_f32_e32 v3, 0x4f7ffffe, v3
	v_cvt_u32_f32_e32 v3, v3
	v_mul_lo_u32 v6, v6, v3
	v_mul_hi_u32 v6, v3, v6
	v_add_u32_e32 v3, v3, v6
	v_mul_hi_u32 v3, v5, v3
	v_mul_lo_u32 v6, v3, v4
	v_sub_u32_e32 v6, v5, v6
	v_cmp_ge_u32_e32 vcc, v6, v4
	v_add_u32_e32 v7, 1, v3
	s_nop 0
	v_cndmask_b32_e32 v3, v3, v7, vcc
	v_sub_u32_e32 v7, v6, v4
	v_cndmask_b32_e32 v6, v6, v7, vcc
	v_cmp_ge_u32_e32 vcc, v6, v4
	v_add_u32_e32 v6, 1, v3
	s_nop 0
	v_cndmask_b32_e32 v3, v3, v6, vcc
	v_add_u32_e32 v6, 1, v5
	v_mad_u64_u32 v[4:5], s[2:3], v4, v3, v[4:5]
	v_cmp_ne_u32_e32 vcc, v6, v4
	s_and_saveexec_b64 s[2:3], vcc
	s_xor_b64 s[2:3], exec, s[2:3]
	s_cbranch_execz .LBB0_926
	s_waitcnt lgkmcnt(0)
	v_mov_b32_e32 v2, 0x2000
	global_load_dword v2, v2, s[0:1] offset:1024 sc1
	s_add_u32 s6, s0, 0x2400
	s_addc_u32 s7, s1, 0
	s_waitcnt vmcnt(0)
	v_cmp_eq_u32_e32 vcc, v2, v3
	s_and_saveexec_b64 s[4:5], vcc
	s_cbranch_execz .LBB0_925
	s_mov_b32 s18, 1
	s_mov_b64 s[8:9], 0
	s_branch .LBB0_916

.LBB0_926:
	s_andn2_saveexec_b64 s[2:3], s[2:3]
	s_cbranch_execz .LBB0_946
	s_mov_b64 s[4:5], exec
	v_cmp_eq_u32_e32 vcc, 0, v20
	s_cbranch_vccz .Lxl_3_full
	v_readlane_b32 s6, v254, 20
	s_cmp_lg_u32 s6, 0
	s_cbranch_scc1 .Lxl_3
.Lxl_3_full:
	buffer_wbl2 sc1
	s_waitcnt lgkmcnt(0)
	s_waitcnt vmcnt(0)
	v_mbcnt_lo_u32_b32 v3, s4, 0
	v_mbcnt_hi_u32_b32 v3, s5, v3
	v_cmp_eq_u32_e32 vcc, 0, v3
	s_and_saveexec_b64 s[6:7], vcc
	s_cbranch_execz .LBB0_929
	s_bcnt1_i32_b64 s4, s[4:5]
	v_mov_b32_e32 v4, s4
	v_readlane_b32 s4, v253, 30
	v_readlane_b32 s5, v253, 31
	s_nop 4
	global_atomic_add v4, v195, v4, s[4:5] sc0

.Lxl_3:
	s_mov_b64 s[4:5], exec
	v_mbcnt_lo_u32_b32 v2, s4, 0
	v_mbcnt_hi_u32_b32 v2, s5, v2
	v_cmp_eq_u32_e32 vcc, 0, v2
	s_waitcnt vmcnt(0)
	buffer_inv sc1
	s_and_saveexec_b64 s[6:7], vcc
	s_cbranch_execz .LBB0_945
	s_bcnt1_i32_b64 s4, s[4:5]
	v_mov_b32_e32 v2, s4
	v_mov_b32_e32 v3, 0x2000
	global_atomic_add v3, v2, s[0:1] offset:1024
